# cache-policy: fp8 weight copies of the conversion loops stored non-temporally
# baseline (speedup 1.0000x reference)
.LBB0_571:
	v_ashrrev_i32_e32 v139, 31, v138
	v_lshlrev_b64 v[138:139], 10, v[138:139]
	s_add_i32 s30, s30, s27
	v_readlane_b32 s6, v254, 46
	v_lshl_add_u64 v[138:139], s[16:17], 0, v[138:139]
	s_add_i32 s24, s24, s25
	s_add_i32 s26, s26, s27
	s_add_i32 s36, s36, s28
	s_add_i32 s29, s29, s27
	s_add_i32 s6, s6, s30
	v_lshl_add_u64 v[138:139], v[138:139], 0, s[14:15]
	s_cmpk_gt_i32 s6, 0x112c
	v_lshl_add_u64 v[138:139], v[138:139], 0, v[136:137]
	s_cselect_b64 s[6:7], -1, 0
	s_waitcnt lgkmcnt(0)
	global_store_dwordx4 v[138:139], v[130:133], off nt

.LBB0_586:
	v_ashrrev_i32_e32 v139, 31, v138
	v_lshlrev_b64 v[138:139], 10, v[138:139]
	v_lshl_add_u64 v[138:139], s[10:11], 0, v[138:139]
	v_lshl_add_u64 v[138:139], v[138:139], 0, s[70:71]
	v_lshl_add_u64 v[138:139], v[138:139], 0, v[136:137]
	s_waitcnt lgkmcnt(0)
	global_store_dwordx4 v[138:139], v[130:133], off nt
	ds_read_b128 v[130:133], v146
	v_cndmask_b32_e64 v0, 0, 1, s[20:21]
	v_cmp_ne_u32_e64 s[6:7], 1, v0
	s_andn2_b64 vcc, exec, s[20:21]
	v_add_u32_e32 v138, s8, v141
	s_cbranch_vccnz .LBB0_592
	v_cmp_lt_i32_e32 vcc, s47, v138
	v_lshlrev_b32_e32 v0, 1, v138
	v_and_b32_e32 v139, 0x7f, v138
	s_and_saveexec_b64 s[20:21], vcc
	s_xor_b64 s[20:21], exec, s[20:21]
	v_add_u32_e32 v0, 0x7ffff800, v0
	v_and_b32_e32 v0, 0x7fffff00, v0
	v_or3_b32 v138, v139, v0, s64
	s_andn2_saveexec_b64 s[20:21], s[20:21]
	v_and_or_b32 v138, v0, s65, v139
	s_or_b64 exec, exec, s[20:21]
.LBB0_592:
	v_ashrrev_i32_e32 v139, 31, v138
	v_lshlrev_b64 v[138:139], 10, v[138:139]
	v_lshl_add_u64 v[138:139], s[10:11], 0, v[138:139]
	v_lshl_add_u64 v[138:139], v[138:139], 0, s[70:71]
	v_lshl_add_u64 v[138:139], v[138:139], 0, v[136:137]
	s_waitcnt lgkmcnt(0)
	global_store_dwordx4 v[138:139], v[130:133], off nt
	ds_read_b128 v[130:133], v147
	v_add_u32_e32 v138, s8, v142
	s_and_b64 vcc, exec, s[6:7]
	s_cbranch_vccnz .LBB0_598
	v_cmp_lt_i32_e32 vcc, s47, v138
	v_lshlrev_b32_e32 v0, 1, v138
	v_and_b32_e32 v139, 0x7f, v138
	s_and_saveexec_b64 s[20:21], vcc
	s_xor_b64 s[20:21], exec, s[20:21]
	v_add_u32_e32 v0, 0x7ffff800, v0
	v_and_b32_e32 v0, 0x7fffff00, v0
	v_or3_b32 v138, v139, v0, s64
	s_andn2_saveexec_b64 s[20:21], s[20:21]
	v_and_or_b32 v138, v0, s65, v139
	s_or_b64 exec, exec, s[20:21]
.LBB0_598:
	v_ashrrev_i32_e32 v139, 31, v138
	v_lshlrev_b64 v[138:139], 10, v[138:139]
	v_lshl_add_u64 v[138:139], s[10:11], 0, v[138:139]
	v_lshl_add_u64 v[138:139], v[138:139], 0, s[70:71]
	v_lshl_add_u64 v[138:139], v[138:139], 0, v[136:137]
	s_waitcnt lgkmcnt(0)
	global_store_dwordx4 v[138:139], v[130:133], off nt
	ds_read_b128 v[130:133], v148
	v_add_u32_e32 v138, s8, v143
	s_and_b64 vcc, exec, s[6:7]
	s_cbranch_vccnz .LBB0_604
	v_cmp_lt_i32_e32 vcc, s47, v138
	v_lshlrev_b32_e32 v0, 1, v138
	v_and_b32_e32 v139, 0x7f, v138
	s_and_saveexec_b64 s[6:7], vcc
	s_xor_b64 s[6:7], exec, s[6:7]
	v_add_u32_e32 v0, 0x7ffff800, v0
	v_and_b32_e32 v0, 0x7fffff00, v0
	v_or3_b32 v138, v139, v0, s64
	s_andn2_saveexec_b64 s[6:7], s[6:7]
	v_and_or_b32 v138, v0, s65, v139
	s_or_b64 exec, exec, s[6:7]
.LBB0_604:
	v_ashrrev_i32_e32 v139, 31, v138
	v_lshlrev_b64 v[138:139], 10, v[138:139]
	v_lshl_add_u64 v[138:139], s[10:11], 0, v[138:139]
	v_lshl_add_u64 v[138:139], v[138:139], 0, s[70:71]
	v_lshl_add_u64 v[138:139], v[138:139], 0, v[136:137]
	s_andn2_b64 vcc, exec, s[18:19]
	s_mov_b64 s[6:7], -1
	s_waitcnt lgkmcnt(0)
	global_store_dwordx4 v[138:139], v[130:133], off nt
	s_cbranch_vccnz .LBB0_572
	v_readlane_b32 s6, v254, 46
	s_add_i32 s6, s6, s26
	s_add_i32 s20, s9, s22
	s_add_i32 s7, s6, 0xd25
	s_cmpk_gt_i32 s7, 0x112c
	s_cbranch_scc1 .LBB0_612
	s_mul_hi_i32 s7, s7, 0x2aaaaaab
	s_lshr_b32 s8, s7, 31
	s_ashr_i32 s13, s7, 9
	s_add_i32 s13, s13, s8
	s_mul_i32 s7, s13, 0xfffff400
	s_add_i32 s21, s6, s7
	s_add_i32 s15, s21, 0xd25
	s_cmpk_gt_i32 s15, 0x7ff
	s_mov_b64 s[18:19], -1
	s_cbranch_scc0 .LBB0_608
	s_addk_i32 s21, 0x525
	s_mov_b32 s10, 31
	s_lshl_b32 s6, s13, 5
	s_lshr_b32 s7, s21, 5
	s_ashr_i32 s11, s10, 31
	s_add_i32 s6, s7, s6
	s_lshl_b32 s9, s20, 5
	s_and_b32 s8, s24, 0x300
	s_lshl_b64 s[10:11], s[10:11], 3
	s_add_u32 s10, s0, s10
	s_addc_u32 s11, s1, s11
	s_load_dwordx2 s[10:11], s[10:11], 0x0
	s_ashr_i32 s7, s6, 31
	s_lshl_b64 s[18:19], s[6:7], 20
	s_lshl_b64 s[6:7], s[6:7], 22
	s_waitcnt lgkmcnt(0)
	s_add_u32 s6, s10, s6
	s_mov_b32 s10, 35
	s_addc_u32 s7, s11, s7
	s_ashr_i32 s11, s10, 31
	s_lshl_b64 s[10:11], s[10:11], 3
	s_add_u32 s10, s0, s10
	s_addc_u32 s11, s1, s11
	s_load_dwordx2 s[10:11], s[10:11], 0x0
	s_waitcnt lgkmcnt(0)
	s_add_u32 s10, s10, s18
	s_addc_u32 s11, s11, s19
	s_add_u32 s10, s10, 0x12800000
	s_addc_u32 s11, s11, 0
	s_mov_b64 s[18:19], 0

.LBB0_618:
	v_ashrrev_i32_e32 v139, 31, v138
	v_lshlrev_b64 v[138:139], 10, v[138:139]
	v_lshl_add_u64 v[138:139], s[16:17], 0, v[138:139]
	s_mov_b32 s15, s71
	v_lshl_add_u64 v[138:139], v[138:139], 0, s[14:15]
	v_lshl_add_u64 v[138:139], v[138:139], 0, v[136:137]
	s_waitcnt lgkmcnt(0)
	global_store_dwordx4 v[138:139], v[130:133], off nt
	ds_read_b128 v[130:133], v146 offset:32768
	v_cndmask_b32_e64 v0, 0, 1, s[18:19]
	v_cmp_ne_u32_e64 s[6:7], 1, v0
	s_andn2_b64 vcc, exec, s[18:19]
	v_add_u32_e32 v138, s12, v141
	s_cbranch_vccnz .LBB0_624
	v_cmp_lt_i32_e32 vcc, s47, v138
	v_lshlrev_b32_e32 v0, 1, v138
	v_and_b32_e32 v139, 0x7f, v138
	s_and_saveexec_b64 s[18:19], vcc
	s_xor_b64 s[18:19], exec, s[18:19]
	v_add_u32_e32 v0, 0x7ffff800, v0
	v_and_b32_e32 v0, 0x7fffff00, v0
	v_or3_b32 v138, v139, v0, s64
	s_andn2_saveexec_b64 s[18:19], s[18:19]
	v_and_or_b32 v138, v0, s65, v139
	s_or_b64 exec, exec, s[18:19]
.LBB0_624:
	v_ashrrev_i32_e32 v139, 31, v138
	v_lshlrev_b64 v[138:139], 10, v[138:139]
	v_lshl_add_u64 v[138:139], s[16:17], 0, v[138:139]
	v_lshl_add_u64 v[138:139], v[138:139], 0, s[14:15]
	v_lshl_add_u64 v[138:139], v[138:139], 0, v[136:137]
	s_waitcnt lgkmcnt(0)
	global_store_dwordx4 v[138:139], v[130:133], off nt
	ds_read_b128 v[130:133], v147 offset:32768
	v_add_u32_e32 v138, s12, v142
	s_and_b64 vcc, exec, s[6:7]
	s_cbranch_vccnz .LBB0_630
	v_cmp_lt_i32_e32 vcc, s47, v138
	v_lshlrev_b32_e32 v0, 1, v138
	v_and_b32_e32 v139, 0x7f, v138
	s_and_saveexec_b64 s[18:19], vcc
	s_xor_b64 s[18:19], exec, s[18:19]
	v_add_u32_e32 v0, 0x7ffff800, v0
	v_and_b32_e32 v0, 0x7fffff00, v0
	v_or3_b32 v138, v139, v0, s64
	s_andn2_saveexec_b64 s[18:19], s[18:19]
	v_and_or_b32 v138, v0, s65, v139
	s_or_b64 exec, exec, s[18:19]
.LBB0_630:
	v_ashrrev_i32_e32 v139, 31, v138
	v_lshlrev_b64 v[138:139], 10, v[138:139]
	v_lshl_add_u64 v[138:139], s[16:17], 0, v[138:139]
	v_lshl_add_u64 v[138:139], v[138:139], 0, s[14:15]
	v_lshl_add_u64 v[138:139], v[138:139], 0, v[136:137]
	s_waitcnt lgkmcnt(0)
	global_store_dwordx4 v[138:139], v[130:133], off nt
	ds_read_b128 v[130:133], v148 offset:32768
	v_add_u32_e32 v138, s12, v143
	s_and_b64 vcc, exec, s[6:7]
	s_cbranch_vccnz .LBB0_571
	v_cmp_lt_i32_e32 vcc, s47, v138
	v_lshlrev_b32_e32 v0, 1, v138
	v_and_b32_e32 v139, 0x7f, v138
	s_and_saveexec_b64 s[6:7], vcc
	s_xor_b64 s[6:7], exec, s[6:7]
	v_add_u32_e32 v0, 0x7ffff800, v0
	v_and_b32_e32 v0, 0x7fffff00, v0
	v_or3_b32 v138, v139, v0, s64
	s_andn2_saveexec_b64 s[6:7], s[6:7]
	s_cbranch_execz .LBB0_570
	v_and_or_b32 v138, v0, s65, v139
	s_branch .LBB0_570

.LBB0_646:
	v_ashrrev_i32_e32 v139, 31, v138
	v_lshlrev_b64 v[138:139], 10, v[138:139]
	s_add_i32 s35, s35, s27
	v_readlane_b32 s6, v254, 46
	v_lshl_add_u64 v[138:139], s[16:17], 0, v[138:139]
	s_add_i32 s24, s24, s25
	s_add_i32 s26, s26, s27
	s_add_i32 s37, s37, s29
	s_add_i32 s30, s30, s27
	s_add_i32 s6, s6, s35
	v_lshl_add_u64 v[138:139], v[138:139], 0, s[14:15]
	s_cmpk_gt_i32 s6, 0x351
	v_lshl_add_u64 v[138:139], v[138:139], 0, v[136:137]
	s_cselect_b64 s[6:7], -1, 0
	s_waitcnt lgkmcnt(0)
	global_store_dwordx4 v[138:139], v[130:133], off nt

.LBB0_679:
	v_ashrrev_i32_e32 v139, 31, v138
	v_lshlrev_b64 v[138:139], 10, v[138:139]
	v_lshl_add_u64 v[138:139], s[10:11], 0, v[138:139]
	v_lshl_add_u64 v[138:139], v[138:139], 0, s[70:71]
	v_lshl_add_u64 v[138:139], v[138:139], 0, v[136:137]
	s_andn2_b64 vcc, exec, s[18:19]
	s_mov_b64 s[6:7], -1
	s_waitcnt lgkmcnt(0)
	global_store_dwordx4 v[138:139], v[130:133], off nt
	s_cbranch_vccnz .LBB0_647
	v_readlane_b32 s6, v254, 46
	s_add_i32 s6, s6, s26
	s_add_i32 s23, s9, s22
	s_sub_i32 s7, s6, 32
	s_cmpk_gt_i32 s7, 0x351
	s_cbranch_scc1 .LBB0_687
	s_mul_hi_i32 s7, s7, 0x2aaaaaab
	s_lshr_b32 s8, s7, 31
	s_ashr_i32 s13, s7, 9
	s_add_i32 s13, s13, s8
	s_mul_i32 s7, s13, 0xfffff400
	s_add_i32 s20, s6, s7
	s_sub_i32 s15, s20, 32
	s_cmpk_gt_i32 s15, 0x7ff
	s_mov_b64 s[18:19], -1
	s_cbranch_scc0 .LBB0_683
	s_addk_i32 s20, 0xf7e0
	s_mov_b32 s10, 31
	s_lshl_b32 s6, s13, 5
	s_lshr_b32 s7, s20, 5
	s_ashr_i32 s11, s10, 31
	s_add_i32 s6, s7, s6
	s_lshl_b32 s9, s23, 5
	s_and_b32 s8, s24, 0x300
	s_lshl_b64 s[10:11], s[10:11], 3
	s_add_u32 s10, s0, s10
	s_addc_u32 s11, s1, s11
	s_load_dwordx2 s[10:11], s[10:11], 0x0
	s_ashr_i32 s7, s6, 31
	s_lshl_b64 s[18:19], s[6:7], 20
	s_lshl_b64 s[6:7], s[6:7], 22
	s_waitcnt lgkmcnt(0)
	s_add_u32 s6, s10, s6
	s_mov_b32 s10, 35
	s_addc_u32 s7, s11, s7
	s_ashr_i32 s11, s10, 31
	s_lshl_b64 s[10:11], s[10:11], 3
	s_add_u32 s10, s0, s10
	s_addc_u32 s11, s1, s11
	s_load_dwordx2 s[10:11], s[10:11], 0x0
	s_waitcnt lgkmcnt(0)
	s_add_u32 s10, s10, s18
	s_addc_u32 s11, s11, s19
	s_add_u32 s10, s10, 0x12800000
	s_addc_u32 s11, s11, 0
	s_mov_b64 s[18:19], 0

.LBB0_988:
	v_ashrrev_i32_e32 v139, 31, v138
	v_lshlrev_b64 v[138:139], 10, v[138:139]
	v_lshl_add_u64 v[138:139], s[28:29], 0, v[138:139]
	v_lshl_add_u64 v[138:139], v[138:139], 0, s[26:27]
	v_lshl_add_u64 v[138:139], v[138:139], 0, v[136:137]
	s_add_i32 s41, s41, 2
	s_add_i32 s40, s40, 32
	s_addk_i32 s37, 0x200
	s_waitcnt lgkmcnt(0)
	global_store_dwordx4 v[138:139], v[130:133], off nt

.LBB0_1003:
	v_ashrrev_i32_e32 v139, 31, v138
	v_lshlrev_b64 v[138:139], 10, v[138:139]
	v_lshl_add_u64 v[138:139], s[12:13], 0, v[138:139]
	v_lshl_add_u64 v[138:139], v[138:139], 0, s[70:71]
	v_lshl_add_u64 v[138:139], v[138:139], 0, v[136:137]
	s_waitcnt lgkmcnt(0)
	global_store_dwordx4 v[138:139], v[130:133], off nt
	ds_read_b128 v[130:133], v146
	v_cndmask_b32_e64 v0, 0, 1, s[34:35]
	v_cmp_ne_u32_e64 s[8:9], 1, v0
	s_andn2_b64 vcc, exec, s[34:35]
	v_add_u32_e32 v138, s10, v141
	s_cbranch_vccnz .LBB0_1009
	v_cmp_lt_i32_e32 vcc, s47, v138
	v_lshlrev_b32_e32 v0, 1, v138
	v_and_b32_e32 v139, 0x7f, v138
	s_and_saveexec_b64 s[34:35], vcc
	s_xor_b64 s[34:35], exec, s[34:35]
	v_add_u32_e32 v0, 0x7ffff800, v0
	v_and_b32_e32 v0, 0x7fffff00, v0
	v_or3_b32 v138, v139, v0, s64
	s_andn2_saveexec_b64 s[34:35], s[34:35]
	v_and_or_b32 v138, v0, s65, v139
	s_or_b64 exec, exec, s[34:35]
.LBB0_1009:
	v_ashrrev_i32_e32 v139, 31, v138
	v_lshlrev_b64 v[138:139], 10, v[138:139]
	v_lshl_add_u64 v[138:139], s[12:13], 0, v[138:139]
	v_lshl_add_u64 v[138:139], v[138:139], 0, s[70:71]
	v_lshl_add_u64 v[138:139], v[138:139], 0, v[136:137]
	s_waitcnt lgkmcnt(0)
	global_store_dwordx4 v[138:139], v[130:133], off nt
	ds_read_b128 v[130:133], v147
	v_add_u32_e32 v138, s10, v142
	s_and_b64 vcc, exec, s[8:9]
	s_cbranch_vccnz .LBB0_1015
	v_cmp_lt_i32_e32 vcc, s47, v138
	v_lshlrev_b32_e32 v0, 1, v138
	v_and_b32_e32 v139, 0x7f, v138
	s_and_saveexec_b64 s[34:35], vcc
	s_xor_b64 s[34:35], exec, s[34:35]
	v_add_u32_e32 v0, 0x7ffff800, v0
	v_and_b32_e32 v0, 0x7fffff00, v0
	v_or3_b32 v138, v139, v0, s64
	s_andn2_saveexec_b64 s[34:35], s[34:35]
	v_and_or_b32 v138, v0, s65, v139
	s_or_b64 exec, exec, s[34:35]
.LBB0_1015:
	v_ashrrev_i32_e32 v139, 31, v138
	v_lshlrev_b64 v[138:139], 10, v[138:139]
	v_lshl_add_u64 v[138:139], s[12:13], 0, v[138:139]
	v_lshl_add_u64 v[138:139], v[138:139], 0, s[70:71]
	v_lshl_add_u64 v[138:139], v[138:139], 0, v[136:137]
	s_waitcnt lgkmcnt(0)
	global_store_dwordx4 v[138:139], v[130:133], off nt
	ds_read_b128 v[130:133], v148
	v_add_u32_e32 v138, s10, v143
	s_and_b64 vcc, exec, s[8:9]
	s_cbranch_vccnz .LBB0_1021
	v_cmp_lt_i32_e32 vcc, s47, v138
	v_lshlrev_b32_e32 v0, 1, v138
	v_and_b32_e32 v139, 0x7f, v138
	s_and_saveexec_b64 s[8:9], vcc
	s_xor_b64 s[8:9], exec, s[8:9]
	v_add_u32_e32 v0, 0x7ffff800, v0
	v_and_b32_e32 v0, 0x7fffff00, v0
	v_or3_b32 v138, v139, v0, s64
	s_andn2_saveexec_b64 s[8:9], s[8:9]
	v_and_or_b32 v138, v0, s65, v139
	s_or_b64 exec, exec, s[8:9]
.LBB0_1021:
	v_ashrrev_i32_e32 v139, 31, v138
	v_lshlrev_b64 v[138:139], 10, v[138:139]
	v_lshl_add_u64 v[138:139], s[12:13], 0, v[138:139]
	v_lshl_add_u64 v[138:139], v[138:139], 0, s[70:71]
	v_lshl_add_u64 v[138:139], v[138:139], 0, v[136:137]
	s_andn2_b64 vcc, exec, s[30:31]
	s_mov_b64 s[30:31], -1
	s_waitcnt lgkmcnt(0)
	global_store_dwordx4 v[138:139], v[130:133], off nt
	s_cbranch_vccnz .LBB0_989
	s_add_i32 s44, s44, 2
	s_cmp_ge_i32 s41, s75
	s_cselect_b64 s[30:31], -1, 0
	s_and_b64 vcc, exec, s[30:31]
	s_cbranch_vccnz .LBB0_1029
	s_mul_hi_i32 s8, s41, 0x2aaaaaab
	s_lshr_b32 s9, s8, 31
	s_ashr_i32 s25, s8, 9
	s_add_i32 s25, s25, s9
	s_mul_i32 s8, s25, 0xfffff400
	s_add_i32 s27, s41, s8
	s_cmpk_gt_i32 s27, 0x7ff
	s_mov_b64 s[34:35], -1
	s_cbranch_scc0 .LBB0_1025
	s_add_i32 s8, s27, 0xfffff800
	s_mov_b32 s12, 31
	s_lshl_b32 s9, s25, 5
	s_lshr_b32 s8, s8, 5
	s_ashr_i32 s13, s12, 31
	s_add_i32 s8, s8, s9
	s_lshl_b32 s11, s44, 5
	s_and_b32 s10, s37, 0x300
	s_lshl_b64 s[12:13], s[12:13], 3
	s_add_u32 s12, s0, s12
	s_addc_u32 s13, s1, s13
	s_load_dwordx2 s[12:13], s[12:13], 0x0
	s_ashr_i32 s9, s8, 31
	s_lshl_b64 s[34:35], s[8:9], 20
	s_lshl_b64 s[8:9], s[8:9], 22
	s_waitcnt lgkmcnt(0)
	s_add_u32 s8, s12, s8
	s_mov_b32 s12, 35
	s_addc_u32 s9, s13, s9
	s_ashr_i32 s13, s12, 31
	s_lshl_b64 s[12:13], s[12:13], 3
	s_add_u32 s12, s0, s12
	s_addc_u32 s13, s1, s13
	s_load_dwordx2 s[12:13], s[12:13], 0x0
	s_waitcnt lgkmcnt(0)
	s_add_u32 s12, s12, s34
	s_addc_u32 s13, s13, s35
	s_add_u32 s12, s12, 0x12800000
	s_addc_u32 s13, s13, 0
	s_mov_b64 s[34:35], 0

.LBB0_1035:
	v_ashrrev_i32_e32 v139, 31, v138
	v_lshlrev_b64 v[138:139], 10, v[138:139]
	v_lshl_add_u64 v[138:139], s[28:29], 0, v[138:139]
	s_mov_b32 s27, s71
	v_lshl_add_u64 v[138:139], v[138:139], 0, s[26:27]
	v_lshl_add_u64 v[138:139], v[138:139], 0, v[136:137]
	s_waitcnt lgkmcnt(0)
	global_store_dwordx4 v[138:139], v[130:133], off nt
	ds_read_b128 v[130:133], v146 offset:32768
	v_cndmask_b32_e64 v0, 0, 1, s[34:35]
	v_cmp_ne_u32_e64 s[8:9], 1, v0
	s_andn2_b64 vcc, exec, s[34:35]
	v_add_u32_e32 v138, s24, v141
	s_cbranch_vccnz .LBB0_1041
	v_cmp_lt_i32_e32 vcc, s47, v138
	v_lshlrev_b32_e32 v0, 1, v138
	v_and_b32_e32 v139, 0x7f, v138
	s_and_saveexec_b64 s[34:35], vcc
	s_xor_b64 s[34:35], exec, s[34:35]
	v_add_u32_e32 v0, 0x7ffff800, v0
	v_and_b32_e32 v0, 0x7fffff00, v0
	v_or3_b32 v138, v139, v0, s64
	s_andn2_saveexec_b64 s[34:35], s[34:35]
	v_and_or_b32 v138, v0, s65, v139
	s_or_b64 exec, exec, s[34:35]
.LBB0_1041:
	v_ashrrev_i32_e32 v139, 31, v138
	v_lshlrev_b64 v[138:139], 10, v[138:139]
	v_lshl_add_u64 v[138:139], s[28:29], 0, v[138:139]
	v_lshl_add_u64 v[138:139], v[138:139], 0, s[26:27]
	v_lshl_add_u64 v[138:139], v[138:139], 0, v[136:137]
	s_waitcnt lgkmcnt(0)
	global_store_dwordx4 v[138:139], v[130:133], off nt
	ds_read_b128 v[130:133], v147 offset:32768
	v_add_u32_e32 v138, s24, v142
	s_and_b64 vcc, exec, s[8:9]
	s_cbranch_vccnz .LBB0_1047
	v_cmp_lt_i32_e32 vcc, s47, v138
	v_lshlrev_b32_e32 v0, 1, v138
	v_and_b32_e32 v139, 0x7f, v138
	s_and_saveexec_b64 s[34:35], vcc
	s_xor_b64 s[34:35], exec, s[34:35]
	v_add_u32_e32 v0, 0x7ffff800, v0
	v_and_b32_e32 v0, 0x7fffff00, v0
	v_or3_b32 v138, v139, v0, s64
	s_andn2_saveexec_b64 s[34:35], s[34:35]
	v_and_or_b32 v138, v0, s65, v139
	s_or_b64 exec, exec, s[34:35]
.LBB0_1047:
	v_ashrrev_i32_e32 v139, 31, v138
	v_lshlrev_b64 v[138:139], 10, v[138:139]
	v_lshl_add_u64 v[138:139], s[28:29], 0, v[138:139]
	v_lshl_add_u64 v[138:139], v[138:139], 0, s[26:27]
	v_lshl_add_u64 v[138:139], v[138:139], 0, v[136:137]
	s_waitcnt lgkmcnt(0)
	global_store_dwordx4 v[138:139], v[130:133], off nt
	ds_read_b128 v[130:133], v148 offset:32768
	v_add_u32_e32 v138, s24, v143
	s_and_b64 vcc, exec, s[8:9]
	s_cbranch_vccnz .LBB0_988
	v_cmp_lt_i32_e32 vcc, s47, v138
	v_lshlrev_b32_e32 v0, 1, v138
	v_and_b32_e32 v139, 0x7f, v138
	s_and_saveexec_b64 s[8:9], vcc
	s_xor_b64 s[8:9], exec, s[8:9]
	v_add_u32_e32 v0, 0x7ffff800, v0
	v_and_b32_e32 v0, 0x7fffff00, v0
	v_or3_b32 v138, v139, v0, s64
	s_andn2_saveexec_b64 s[8:9], s[8:9]
	s_cbranch_execz .LBB0_987
	v_and_or_b32 v138, v0, s65, v139
	s_branch .LBB0_987

.LBB0_1414:
	v_ashrrev_i32_e32 v139, 31, v138
	v_lshlrev_b64 v[138:139], 10, v[138:139]
	s_add_i32 s31, s31, s26
	v_readlane_b32 s6, v254, 46
	v_lshl_add_u64 v[138:139], s[16:17], 0, v[138:139]
	s_add_i32 s22, s22, s24
	s_add_i32 s25, s25, s26
	s_add_i32 s35, s35, s28
	s_add_i32 s29, s29, s26
	s_add_i32 s6, s6, s31
	v_lshl_add_u64 v[138:139], v[138:139], 0, s[14:15]
	s_cmpk_gt_i32 s6, 0xd44
	v_lshl_add_u64 v[138:139], v[138:139], 0, v[136:137]
	s_cselect_b64 s[6:7], -1, 0
	s_waitcnt lgkmcnt(0)
	global_store_dwordx4 v[138:139], v[130:133], off nt

.LBB0_1447:
	v_ashrrev_i32_e32 v139, 31, v138
	v_lshlrev_b64 v[138:139], 10, v[138:139]
	v_lshl_add_u64 v[138:139], s[10:11], 0, v[138:139]
	v_lshl_add_u64 v[138:139], v[138:139], 0, s[70:71]
	v_lshl_add_u64 v[138:139], v[138:139], 0, v[136:137]
	s_andn2_b64 vcc, exec, s[18:19]
	s_mov_b64 s[6:7], -1
	s_waitcnt lgkmcnt(0)
	global_store_dwordx4 v[138:139], v[130:133], off nt
	s_cbranch_vccnz .LBB0_1415
	v_readlane_b32 s6, v254, 46
	s_add_i32 s6, s6, s25
	s_add_i32 s20, s9, s23
	s_add_i32 s7, s6, 0xa05
	s_cmpk_gt_i32 s7, 0xd44
	s_cbranch_scc1 .LBB0_1455
	s_mul_hi_i32 s7, s7, 0x2aaaaaab
	s_lshr_b32 s8, s7, 31
	s_ashr_i32 s13, s7, 9
	s_add_i32 s13, s13, s8
	s_mul_i32 s7, s13, 0xfffff400
	s_add_i32 s21, s6, s7
	s_add_i32 s15, s21, 0xa05
	s_cmpk_gt_i32 s15, 0x7ff
	s_mov_b64 s[18:19], -1
	s_cbranch_scc0 .LBB0_1451
	s_addk_i32 s21, 0x205
	s_mov_b32 s10, 31
	s_lshl_b32 s6, s13, 5
	s_lshr_b32 s7, s21, 5
	s_ashr_i32 s11, s10, 31
	s_add_i32 s6, s7, s6
	s_lshl_b32 s9, s20, 5
	s_and_b32 s8, s22, 0x300
	s_lshl_b64 s[10:11], s[10:11], 3
	s_add_u32 s10, s0, s10
	s_addc_u32 s11, s1, s11
	s_load_dwordx2 s[10:11], s[10:11], 0x0
	s_ashr_i32 s7, s6, 31
	s_lshl_b64 s[18:19], s[6:7], 20
	s_lshl_b64 s[6:7], s[6:7], 22
	s_waitcnt lgkmcnt(0)
	s_add_u32 s6, s10, s6
	s_mov_b32 s10, 35
	s_addc_u32 s7, s11, s7
	s_ashr_i32 s11, s10, 31
	s_lshl_b64 s[10:11], s[10:11], 3
	s_add_u32 s10, s0, s10
	s_addc_u32 s11, s1, s11
	s_load_dwordx2 s[10:11], s[10:11], 0x0
	s_waitcnt lgkmcnt(0)
	s_add_u32 s10, s10, s18
	s_addc_u32 s11, s11, s19
	s_add_u32 s10, s10, 0x12800000
	s_addc_u32 s11, s11, 0
	s_mov_b64 s[18:19], 0
